# variant of v28: keep_v32_w1late
# baseline (speedup 1.0000x reference)
.Llstm3_loop:
	ds_read_b128 v[184:187], v209 offset:0
	ds_read_b128 v[188:191], v209 offset:64
	ds_read_b128 v[176:179], v211 offset:0
	ds_read_b128 v[180:183], v211 offset:64
	s_waitcnt lgkmcnt(3)
	v_mfma_f32_16x16x32_f16 v[168:171], v[16:19], v[184:187], v[192:195]
	v_mfma_f32_16x16x32_f16 v[172:175], v[24:27], v[184:187], v[192:195]
	s_waitcnt lgkmcnt(2)
	v_mfma_f32_16x16x32_f16 v[168:171], v[20:23], v[188:191], v[168:171]
	v_mfma_f32_16x16x32_f16 v[172:175], v[28:31], v[188:191], v[172:175]
	s_waitcnt lgkmcnt(1)
	v_mfma_f32_16x16x32_f16 v[168:171], v[32:35], v[176:179], v[168:171]
	v_mfma_f32_16x16x32_f16 v[172:175], v[40:43], v[176:179], v[172:175]
	s_waitcnt lgkmcnt(0)
	v_mfma_f32_16x16x32_f16 v[168:171], v[36:39], v[180:183], v[168:171]
	v_mfma_f32_16x16x32_f16 v[172:175], v[44:47], v[180:183], v[172:175]
	v_max_f32_e32 v221, v221, v215
	v_mfma_f32_16x16x32_f16 v[164:167], v[68:71], v[148:151], v[164:167]
	s_waitcnt vmcnt(4)
	v_mfma_f32_16x16x32_f16 v[160:163], v[60:63], v[156:159], v[160:163]
	s_nop 3
	v_mov_b32_dpp v168, v172 quad_perm:[0,1,2,3] row_mask:0xf bank_mask:0xa
	v_mov_b32_dpp v169, v173 quad_perm:[0,1,2,3] row_mask:0xf bank_mask:0xa
	v_mov_b32_dpp v170, v174 quad_perm:[0,1,2,3] row_mask:0xf bank_mask:0xa
	v_exp_f32_e32 v200, v168
	v_mov_b32_dpp v171, v175 quad_perm:[0,1,2,3] row_mask:0xf bank_mask:0xa
	v_exp_f32_e32 v201, v169
	v_exp_f32_e32 v202, v170
	v_add_f32_e32 v200, 1.0, v200
	v_exp_f32_e32 v203, v171
	v_add_f32_e32 v201, 1.0, v201
	v_add_f32_e32 v202, 1.0, v202
	v_rcp_f32_e32 v202, v202
	v_rcp_f32_e32 v200, v200
	v_rcp_f32_e32 v201, v201
	v_add_f32_e32 v203, 1.0, v203
	v_fmamk_f32 v204, v202, 0xc0b8aa3b, v222
	v_rcp_f32_e32 v203, v203
	v_mul_f32_e32 v205, v200, v204
	v_fma_f32 v220, v201, v220, v205
	v_exp_f32_e32 v206, v220
	v_mul_f32_e32 v207, -2.0, v203
	v_add_f32_e32 v206, 1.0, v206
	v_rcp_f32_e32 v206, v206
	s_nop 0
	v_fma_mixlo_f16 v208, v206, v207, v203
	ds_write_b16 v225, v208 offset:576
	v_fma_f32 v215, v206, v207, v203
	v_mfma_f32_16x16x32_f16 v[232:235], v[80:83], v[144:147], v[120:123]
	v_mfma_f32_16x16x32_f16 v[164:167], v[72:75], v[152:155], v[164:167]
	ds_write_b128 v227, v[160:163] offset:4352
	ds_read_b128 v[196:199], v226 offset:1088
	s_waitcnt lgkmcnt(2)
	s_barrier
	ds_read_b128 v[184:187], v210 offset:576
	ds_read_b128 v[188:191], v210 offset:640
	ds_read_b128 v[176:179], v212 offset:576
	ds_read_b128 v[180:183], v212 offset:640
	s_waitcnt lgkmcnt(3)
	v_mfma_f32_16x16x32_f16 v[168:171], v[16:19], v[184:187], v[196:199]
	v_mfma_f32_16x16x32_f16 v[172:175], v[24:27], v[184:187], v[196:199]
	s_waitcnt lgkmcnt(2)
	v_mfma_f32_16x16x32_f16 v[168:171], v[20:23], v[188:191], v[168:171]
	v_mfma_f32_16x16x32_f16 v[172:175], v[28:31], v[188:191], v[172:175]
	s_waitcnt lgkmcnt(1)
	v_mfma_f32_16x16x32_f16 v[168:171], v[32:35], v[176:179], v[168:171]
	v_mfma_f32_16x16x32_f16 v[172:175], v[40:43], v[176:179], v[172:175]
	s_waitcnt lgkmcnt(0)
	v_mfma_f32_16x16x32_f16 v[168:171], v[36:39], v[180:183], v[168:171]
	v_mfma_f32_16x16x32_f16 v[172:175], v[44:47], v[180:183], v[172:175]
	v_max_f32_e32 v221, v221, v215
	v_mfma_f32_16x16x32_f16 v[232:235], v[84:87], v[148:151], v[232:235]
	v_mfma_f32_16x16x32_f16 v[164:167], v[76:79], v[156:159], v[164:167]
	s_nop 4
	v_mov_b32_dpp v168, v172 quad_perm:[0,1,2,3] row_mask:0xf bank_mask:0xa
	v_mov_b32_dpp v169, v173 quad_perm:[0,1,2,3] row_mask:0xf bank_mask:0xa
	v_mov_b32_dpp v170, v174 quad_perm:[0,1,2,3] row_mask:0xf bank_mask:0xa
	v_exp_f32_e32 v200, v168
	v_mov_b32_dpp v171, v175 quad_perm:[0,1,2,3] row_mask:0xf bank_mask:0xa
	v_exp_f32_e32 v201, v169
	v_exp_f32_e32 v202, v170
	v_add_f32_e32 v200, 1.0, v200
	v_exp_f32_e32 v203, v171
	v_add_f32_e32 v201, 1.0, v201
	v_add_f32_e32 v202, 1.0, v202
	v_rcp_f32_e32 v202, v202
	v_rcp_f32_e32 v200, v200
	v_rcp_f32_e32 v201, v201
	v_add_f32_e32 v203, 1.0, v203
	v_fmamk_f32 v204, v202, 0xc0b8aa3b, v222
	v_rcp_f32_e32 v203, v203
	v_mul_f32_e32 v205, v200, v204
	v_fma_f32 v220, v201, v220, v205
	v_exp_f32_e32 v206, v220
	v_mul_f32_e32 v207, -2.0, v203
	v_add_f32_e32 v206, 1.0, v206
	v_rcp_f32_e32 v206, v206
	s_nop 0
	v_fma_mixlo_f16 v208, v206, v207, v203
	ds_write_b16 v225, v208 offset:0
	v_fma_f32 v215, v206, v207, v203
	v_mfma_f32_16x16x32_f16 v[236:239], v[96:99], v[144:147], v[124:127]
	v_mfma_f32_16x16x32_f16 v[232:235], v[88:91], v[152:155], v[232:235]
	global_load_dwordx4 v[144:147], v[228:229], off offset:0
	ds_write_b128 v227, v[164:167] offset:4416
	ds_read_b128 v[192:195], v226 offset:2176
	s_waitcnt lgkmcnt(2)
	s_barrier
	ds_read_b128 v[184:187], v209 offset:0
	ds_read_b128 v[188:191], v209 offset:64
	ds_read_b128 v[176:179], v211 offset:0
	ds_read_b128 v[180:183], v211 offset:64
	s_waitcnt lgkmcnt(3)
	v_mfma_f32_16x16x32_f16 v[168:171], v[16:19], v[184:187], v[192:195]
	v_mfma_f32_16x16x32_f16 v[172:175], v[24:27], v[184:187], v[192:195]
	s_waitcnt lgkmcnt(2)
	v_mfma_f32_16x16x32_f16 v[168:171], v[20:23], v[188:191], v[168:171]
	v_mfma_f32_16x16x32_f16 v[172:175], v[28:31], v[188:191], v[172:175]
	s_waitcnt lgkmcnt(1)
	v_mfma_f32_16x16x32_f16 v[168:171], v[32:35], v[176:179], v[168:171]
	v_mfma_f32_16x16x32_f16 v[172:175], v[40:43], v[176:179], v[172:175]
	s_waitcnt lgkmcnt(0)
	v_mfma_f32_16x16x32_f16 v[168:171], v[36:39], v[180:183], v[168:171]
	v_mfma_f32_16x16x32_f16 v[172:175], v[44:47], v[180:183], v[172:175]
	v_max_f32_e32 v221, v221, v215
	v_mfma_f32_16x16x32_f16 v[236:239], v[100:103], v[148:151], v[236:239]
	v_mfma_f32_16x16x32_f16 v[232:235], v[92:95], v[156:159], v[232:235]
	global_load_dwordx4 v[148:151], v[228:229], off offset:64
	s_nop 3
	v_mov_b32_dpp v168, v172 quad_perm:[0,1,2,3] row_mask:0xf bank_mask:0xa
	v_mov_b32_dpp v169, v173 quad_perm:[0,1,2,3] row_mask:0xf bank_mask:0xa
	v_mov_b32_dpp v170, v174 quad_perm:[0,1,2,3] row_mask:0xf bank_mask:0xa
	v_exp_f32_e32 v200, v168
	v_mov_b32_dpp v171, v175 quad_perm:[0,1,2,3] row_mask:0xf bank_mask:0xa
	v_exp_f32_e32 v201, v169
	v_exp_f32_e32 v202, v170
	v_add_f32_e32 v200, 1.0, v200
	v_exp_f32_e32 v203, v171
	v_add_f32_e32 v201, 1.0, v201
	v_add_f32_e32 v202, 1.0, v202
	v_rcp_f32_e32 v202, v202
	v_rcp_f32_e32 v200, v200
	v_rcp_f32_e32 v201, v201
	v_add_f32_e32 v203, 1.0, v203
	v_fmamk_f32 v204, v202, 0xc0b8aa3b, v222
	v_rcp_f32_e32 v203, v203
	v_mul_f32_e32 v205, v200, v204
	v_fma_f32 v220, v201, v220, v205
	v_exp_f32_e32 v206, v220
	v_mul_f32_e32 v207, -2.0, v203
	v_add_f32_e32 v206, 1.0, v206
	v_rcp_f32_e32 v206, v206
	s_nop 0
	v_fma_mixlo_f16 v208, v206, v207, v203
	ds_write_b16 v225, v208 offset:576
	v_fma_f32 v215, v206, v207, v203
	s_waitcnt vmcnt(5)
	v_mfma_f32_16x16x32_f16 v[160:163], v[48:51], v[128:131], v[112:115]
	v_mfma_f32_16x16x32_f16 v[236:239], v[104:107], v[152:155], v[236:239]
	global_load_dwordx4 v[152:155], v[228:229], off offset:128
	ds_write_b128 v227, v[232:235] offset:4480
	ds_read_b128 v[196:199], v226 offset:3264
	s_waitcnt lgkmcnt(2)
	s_barrier
	ds_read_b128 v[184:187], v210 offset:576
	ds_read_b128 v[188:191], v210 offset:640
	ds_read_b128 v[176:179], v212 offset:576
	ds_read_b128 v[180:183], v212 offset:640
	s_waitcnt lgkmcnt(3)
	v_mfma_f32_16x16x32_f16 v[168:171], v[16:19], v[184:187], v[196:199]
	v_mfma_f32_16x16x32_f16 v[172:175], v[24:27], v[184:187], v[196:199]
	s_waitcnt lgkmcnt(2)
	v_mfma_f32_16x16x32_f16 v[168:171], v[20:23], v[188:191], v[168:171]
	v_mfma_f32_16x16x32_f16 v[172:175], v[28:31], v[188:191], v[172:175]
	s_waitcnt lgkmcnt(1)
	v_mfma_f32_16x16x32_f16 v[168:171], v[32:35], v[176:179], v[168:171]
	v_mfma_f32_16x16x32_f16 v[172:175], v[40:43], v[176:179], v[172:175]
	s_waitcnt lgkmcnt(0)
	v_mfma_f32_16x16x32_f16 v[168:171], v[36:39], v[180:183], v[168:171]
	v_mfma_f32_16x16x32_f16 v[172:175], v[44:47], v[180:183], v[172:175]
	v_max_f32_e32 v221, v221, v215
	s_waitcnt vmcnt(5)
	v_mfma_f32_16x16x32_f16 v[160:163], v[52:55], v[132:135], v[160:163]
	v_mfma_f32_16x16x32_f16 v[236:239], v[108:111], v[156:159], v[236:239]
	global_load_dwordx4 v[156:159], v[228:229], off offset:192
	v_lshl_add_u64 v[228:229], v[228:229], 0, s[20:21]
	s_nop 1
	v_mov_b32_dpp v168, v172 quad_perm:[0,1,2,3] row_mask:0xf bank_mask:0xa
	v_mov_b32_dpp v169, v173 quad_perm:[0,1,2,3] row_mask:0xf bank_mask:0xa
	v_mov_b32_dpp v170, v174 quad_perm:[0,1,2,3] row_mask:0xf bank_mask:0xa
	v_exp_f32_e32 v200, v168
	v_mov_b32_dpp v171, v175 quad_perm:[0,1,2,3] row_mask:0xf bank_mask:0xa
	v_exp_f32_e32 v201, v169
	v_exp_f32_e32 v202, v170
	v_add_f32_e32 v200, 1.0, v200
	v_exp_f32_e32 v203, v171
	v_add_f32_e32 v201, 1.0, v201
	v_add_f32_e32 v202, 1.0, v202
	v_rcp_f32_e32 v202, v202
	v_rcp_f32_e32 v200, v200
	v_rcp_f32_e32 v201, v201
	v_add_f32_e32 v203, 1.0, v203
	v_fmamk_f32 v204, v202, 0xc0b8aa3b, v222
	v_rcp_f32_e32 v203, v203
	v_mul_f32_e32 v205, v200, v204
	v_fma_f32 v220, v201, v220, v205
	v_exp_f32_e32 v206, v220
	v_mul_f32_e32 v207, -2.0, v203
	v_add_f32_e32 v206, 1.0, v206
	v_rcp_f32_e32 v206, v206
	s_nop 0
	v_fma_mixlo_f16 v208, v206, v207, v203
	ds_write_b16 v225, v208 offset:0
	v_fma_f32 v215, v206, v207, v203
	v_mfma_f32_16x16x32_f16 v[164:167], v[64:67], v[128:131], v[116:119]
	s_waitcnt vmcnt(5)
	v_mfma_f32_16x16x32_f16 v[160:163], v[56:59], v[136:139], v[160:163]
	ds_write_b128 v227, v[236:239] offset:4544
	ds_read_b128 v[192:195], v226 offset:4352
	s_waitcnt lgkmcnt(2)
	s_barrier
	ds_read_b128 v[184:187], v209 offset:0
	ds_read_b128 v[188:191], v209 offset:64
	ds_read_b128 v[176:179], v211 offset:0
	ds_read_b128 v[180:183], v211 offset:64
	s_waitcnt lgkmcnt(3)
	v_mfma_f32_16x16x32_f16 v[168:171], v[16:19], v[184:187], v[192:195]
	v_mfma_f32_16x16x32_f16 v[172:175], v[24:27], v[184:187], v[192:195]
	s_waitcnt lgkmcnt(2)
	v_mfma_f32_16x16x32_f16 v[168:171], v[20:23], v[188:191], v[168:171]
	v_mfma_f32_16x16x32_f16 v[172:175], v[28:31], v[188:191], v[172:175]
	s_waitcnt lgkmcnt(1)
	v_mfma_f32_16x16x32_f16 v[168:171], v[32:35], v[176:179], v[168:171]
	v_mfma_f32_16x16x32_f16 v[172:175], v[40:43], v[176:179], v[172:175]
	s_waitcnt lgkmcnt(0)
	v_mfma_f32_16x16x32_f16 v[168:171], v[36:39], v[180:183], v[168:171]
	v_mfma_f32_16x16x32_f16 v[172:175], v[44:47], v[180:183], v[172:175]
	v_max_f32_e32 v221, v221, v215
	v_mfma_f32_16x16x32_f16 v[164:167], v[68:71], v[132:135], v[164:167]
	s_waitcnt vmcnt(4)
	v_mfma_f32_16x16x32_f16 v[160:163], v[60:63], v[140:143], v[160:163]
	s_nop 3
	v_mov_b32_dpp v168, v172 quad_perm:[0,1,2,3] row_mask:0xf bank_mask:0xa
	v_mov_b32_dpp v169, v173 quad_perm:[0,1,2,3] row_mask:0xf bank_mask:0xa
	v_mov_b32_dpp v170, v174 quad_perm:[0,1,2,3] row_mask:0xf bank_mask:0xa
	v_exp_f32_e32 v200, v168
	v_mov_b32_dpp v171, v175 quad_perm:[0,1,2,3] row_mask:0xf bank_mask:0xa
	v_exp_f32_e32 v201, v169
	v_exp_f32_e32 v202, v170
	v_add_f32_e32 v200, 1.0, v200
	v_exp_f32_e32 v203, v171
	v_add_f32_e32 v201, 1.0, v201
	v_add_f32_e32 v202, 1.0, v202
	v_rcp_f32_e32 v202, v202
	v_rcp_f32_e32 v200, v200
	v_rcp_f32_e32 v201, v201
	v_add_f32_e32 v203, 1.0, v203
	v_fmamk_f32 v204, v202, 0xc0b8aa3b, v222
	v_rcp_f32_e32 v203, v203
	v_mul_f32_e32 v205, v200, v204
	v_fma_f32 v220, v201, v220, v205
	v_exp_f32_e32 v206, v220
	v_mul_f32_e32 v207, -2.0, v203
	v_add_f32_e32 v206, 1.0, v206
	v_rcp_f32_e32 v206, v206
	s_nop 0
	v_fma_mixlo_f16 v208, v206, v207, v203
	ds_write_b16 v225, v208 offset:576
	v_fma_f32 v215, v206, v207, v203
	v_mfma_f32_16x16x32_f16 v[232:235], v[80:83], v[128:131], v[120:123]
	v_mfma_f32_16x16x32_f16 v[164:167], v[72:75], v[136:139], v[164:167]
	ds_write_b128 v227, v[160:163] offset:0
	ds_read_b128 v[196:199], v226 offset:5440
	s_waitcnt lgkmcnt(2)
	s_barrier
	ds_read_b128 v[184:187], v210 offset:576
	ds_read_b128 v[188:191], v210 offset:640
	ds_read_b128 v[176:179], v212 offset:576
	ds_read_b128 v[180:183], v212 offset:640
	s_waitcnt lgkmcnt(3)
	v_mfma_f32_16x16x32_f16 v[168:171], v[16:19], v[184:187], v[196:199]
	v_mfma_f32_16x16x32_f16 v[172:175], v[24:27], v[184:187], v[196:199]
	s_waitcnt lgkmcnt(2)
	v_mfma_f32_16x16x32_f16 v[168:171], v[20:23], v[188:191], v[168:171]
	v_mfma_f32_16x16x32_f16 v[172:175], v[28:31], v[188:191], v[172:175]
	s_waitcnt lgkmcnt(1)
	v_mfma_f32_16x16x32_f16 v[168:171], v[32:35], v[176:179], v[168:171]
	v_mfma_f32_16x16x32_f16 v[172:175], v[40:43], v[176:179], v[172:175]
	s_waitcnt lgkmcnt(0)
	v_mfma_f32_16x16x32_f16 v[168:171], v[36:39], v[180:183], v[168:171]
	v_mfma_f32_16x16x32_f16 v[172:175], v[44:47], v[180:183], v[172:175]
	v_max_f32_e32 v221, v221, v215
	v_mfma_f32_16x16x32_f16 v[232:235], v[84:87], v[132:135], v[232:235]
	v_mfma_f32_16x16x32_f16 v[164:167], v[76:79], v[140:143], v[164:167]
	s_nop 4
	v_mov_b32_dpp v168, v172 quad_perm:[0,1,2,3] row_mask:0xf bank_mask:0xa
	v_mov_b32_dpp v169, v173 quad_perm:[0,1,2,3] row_mask:0xf bank_mask:0xa
	v_mov_b32_dpp v170, v174 quad_perm:[0,1,2,3] row_mask:0xf bank_mask:0xa
	v_exp_f32_e32 v200, v168
	v_mov_b32_dpp v171, v175 quad_perm:[0,1,2,3] row_mask:0xf bank_mask:0xa
	v_exp_f32_e32 v201, v169
	v_exp_f32_e32 v202, v170
	v_add_f32_e32 v200, 1.0, v200
	v_exp_f32_e32 v203, v171
	v_add_f32_e32 v201, 1.0, v201
	v_add_f32_e32 v202, 1.0, v202
	v_rcp_f32_e32 v202, v202
	v_rcp_f32_e32 v200, v200
	v_rcp_f32_e32 v201, v201
	v_add_f32_e32 v203, 1.0, v203
	v_fmamk_f32 v204, v202, 0xc0b8aa3b, v222
	v_rcp_f32_e32 v203, v203
	v_mul_f32_e32 v205, v200, v204
	v_fma_f32 v220, v201, v220, v205
	v_exp_f32_e32 v206, v220
	v_mul_f32_e32 v207, -2.0, v203
	v_add_f32_e32 v206, 1.0, v206
	v_rcp_f32_e32 v206, v206
	s_nop 0
	v_fma_mixlo_f16 v208, v206, v207, v203
	ds_write_b16 v225, v208 offset:0
	v_fma_f32 v215, v206, v207, v203
	v_mfma_f32_16x16x32_f16 v[236:239], v[96:99], v[128:131], v[124:127]
	v_mfma_f32_16x16x32_f16 v[232:235], v[88:91], v[136:139], v[232:235]
	global_load_dwordx4 v[128:131], v[228:229], off offset:0
	ds_write_b128 v227, v[164:167] offset:64
	ds_read_b128 v[192:195], v226 offset:6528
	s_waitcnt lgkmcnt(2)
	s_barrier
	ds_read_b128 v[184:187], v209 offset:0
	ds_read_b128 v[188:191], v209 offset:64
	ds_read_b128 v[176:179], v211 offset:0
	ds_read_b128 v[180:183], v211 offset:64
	s_waitcnt lgkmcnt(3)
	v_mfma_f32_16x16x32_f16 v[168:171], v[16:19], v[184:187], v[192:195]
	v_mfma_f32_16x16x32_f16 v[172:175], v[24:27], v[184:187], v[192:195]
	s_waitcnt lgkmcnt(2)
	v_mfma_f32_16x16x32_f16 v[168:171], v[20:23], v[188:191], v[168:171]
	v_mfma_f32_16x16x32_f16 v[172:175], v[28:31], v[188:191], v[172:175]
	s_waitcnt lgkmcnt(1)
	v_mfma_f32_16x16x32_f16 v[168:171], v[32:35], v[176:179], v[168:171]
	v_mfma_f32_16x16x32_f16 v[172:175], v[40:43], v[176:179], v[172:175]
	s_waitcnt lgkmcnt(0)
	v_mfma_f32_16x16x32_f16 v[168:171], v[36:39], v[180:183], v[168:171]
	v_mfma_f32_16x16x32_f16 v[172:175], v[44:47], v[180:183], v[172:175]
	v_max_f32_e32 v221, v221, v215
	v_mfma_f32_16x16x32_f16 v[236:239], v[100:103], v[132:135], v[236:239]
	v_mfma_f32_16x16x32_f16 v[232:235], v[92:95], v[140:143], v[232:235]
	global_load_dwordx4 v[132:135], v[228:229], off offset:64
	s_nop 3
	v_mov_b32_dpp v168, v172 quad_perm:[0,1,2,3] row_mask:0xf bank_mask:0xa
	v_mov_b32_dpp v169, v173 quad_perm:[0,1,2,3] row_mask:0xf bank_mask:0xa
	v_mov_b32_dpp v170, v174 quad_perm:[0,1,2,3] row_mask:0xf bank_mask:0xa
	v_exp_f32_e32 v200, v168
	v_mov_b32_dpp v171, v175 quad_perm:[0,1,2,3] row_mask:0xf bank_mask:0xa
	v_exp_f32_e32 v201, v169
	v_exp_f32_e32 v202, v170
	v_add_f32_e32 v200, 1.0, v200
	v_exp_f32_e32 v203, v171
	v_add_f32_e32 v201, 1.0, v201
	v_add_f32_e32 v202, 1.0, v202
	v_rcp_f32_e32 v202, v202
	v_rcp_f32_e32 v200, v200
	v_rcp_f32_e32 v201, v201
	v_add_f32_e32 v203, 1.0, v203
	v_fmamk_f32 v204, v202, 0xc0b8aa3b, v222
	v_rcp_f32_e32 v203, v203
	v_mul_f32_e32 v205, v200, v204
	v_fma_f32 v220, v201, v220, v205
	v_exp_f32_e32 v206, v220
	v_mul_f32_e32 v207, -2.0, v203
	v_add_f32_e32 v206, 1.0, v206
	v_rcp_f32_e32 v206, v206
	s_nop 0
	v_fma_mixlo_f16 v208, v206, v207, v203
	ds_write_b16 v225, v208 offset:576
	v_fma_f32 v215, v206, v207, v203
	s_waitcnt vmcnt(5)
	v_mfma_f32_16x16x32_f16 v[160:163], v[48:51], v[144:147], v[112:115]
	v_mfma_f32_16x16x32_f16 v[236:239], v[104:107], v[136:139], v[236:239]
	global_load_dwordx4 v[136:139], v[228:229], off offset:128
	ds_write_b128 v227, v[232:235] offset:128
	ds_read_b128 v[196:199], v226 offset:7616
	s_waitcnt lgkmcnt(2)
	s_barrier
	ds_read_b128 v[184:187], v210 offset:576
	ds_read_b128 v[188:191], v210 offset:640
	ds_read_b128 v[176:179], v212 offset:576
	ds_read_b128 v[180:183], v212 offset:640
	s_waitcnt lgkmcnt(3)
	v_mfma_f32_16x16x32_f16 v[168:171], v[16:19], v[184:187], v[196:199]
	v_mfma_f32_16x16x32_f16 v[172:175], v[24:27], v[184:187], v[196:199]
	s_waitcnt lgkmcnt(2)
	v_mfma_f32_16x16x32_f16 v[168:171], v[20:23], v[188:191], v[168:171]
	v_mfma_f32_16x16x32_f16 v[172:175], v[28:31], v[188:191], v[172:175]
	s_waitcnt lgkmcnt(1)
	v_mfma_f32_16x16x32_f16 v[168:171], v[32:35], v[176:179], v[168:171]
	v_mfma_f32_16x16x32_f16 v[172:175], v[40:43], v[176:179], v[172:175]
	s_waitcnt lgkmcnt(0)
	v_mfma_f32_16x16x32_f16 v[168:171], v[36:39], v[180:183], v[168:171]
	v_mfma_f32_16x16x32_f16 v[172:175], v[44:47], v[180:183], v[172:175]
	v_max_f32_e32 v221, v221, v215
	s_waitcnt vmcnt(5)
	v_mfma_f32_16x16x32_f16 v[160:163], v[52:55], v[148:151], v[160:163]
	v_mfma_f32_16x16x32_f16 v[236:239], v[108:111], v[140:143], v[236:239]
	global_load_dwordx4 v[140:143], v[228:229], off offset:192
	v_lshl_add_u64 v[228:229], v[228:229], 0, s[20:21]
	s_nop 1
	v_mov_b32_dpp v168, v172 quad_perm:[0,1,2,3] row_mask:0xf bank_mask:0xa
	v_mov_b32_dpp v169, v173 quad_perm:[0,1,2,3] row_mask:0xf bank_mask:0xa
	v_mov_b32_dpp v170, v174 quad_perm:[0,1,2,3] row_mask:0xf bank_mask:0xa
	v_exp_f32_e32 v200, v168
	v_mov_b32_dpp v171, v175 quad_perm:[0,1,2,3] row_mask:0xf bank_mask:0xa
	v_exp_f32_e32 v201, v169
	v_exp_f32_e32 v202, v170
	v_add_f32_e32 v200, 1.0, v200
	v_exp_f32_e32 v203, v171
	v_add_f32_e32 v201, 1.0, v201
	v_add_f32_e32 v202, 1.0, v202
	v_rcp_f32_e32 v202, v202
	v_rcp_f32_e32 v200, v200
	v_rcp_f32_e32 v201, v201
	v_add_f32_e32 v203, 1.0, v203
	v_fmamk_f32 v204, v202, 0xc0b8aa3b, v222
	v_rcp_f32_e32 v203, v203
	v_mul_f32_e32 v205, v200, v204
	v_fma_f32 v220, v201, v220, v205
	v_exp_f32_e32 v206, v220
	v_mul_f32_e32 v207, -2.0, v203
	v_add_f32_e32 v206, 1.0, v206
	v_rcp_f32_e32 v206, v206
	s_nop 0
	v_fma_mixlo_f16 v208, v206, v207, v203
	ds_write_b16 v225, v208 offset:0
	v_fma_f32 v215, v206, v207, v203
	v_mfma_f32_16x16x32_f16 v[164:167], v[64:67], v[144:147], v[116:119]
	s_waitcnt vmcnt(5)
	v_mfma_f32_16x16x32_f16 v[160:163], v[56:59], v[152:155], v[160:163]
	ds_write_b128 v227, v[236:239] offset:192
	ds_read_b128 v[192:195], v226 offset:0
	s_waitcnt lgkmcnt(2)
	s_barrier
	s_sub_u32 s4, s4, 1
	s_cmp_lg_u32 s4, 0
	s_cbranch_scc1 .Llstm3_loop
	v_max_f32_e32 v221, v221, v215
	global_store_dword v230, v221, s[12:13]
	s_endpgm
